# P4 epilogue: second batch of residual loads hoisted next to first batch (v216-v247), same as P7
# baseline (speedup 1.0000x reference)
; #define LAS __attribute__((address_space(3)))
; __device__ __forceinline__ v4u pack8(const f32x4 a, const f32x4 b) { v4u w; w.x = cvt_pk_bf16(a[0], a[1]); w.y = cvt_pk_bf16(a[2], a[3]); w.z = cvt_pk_bf16(b[0], b[1]); w.w = cvt_pk_bf16(b[2], b[3]); return w; }
;     __device__ __forceinline__ void operator()(const Acc& acc, const Unit& u, int wr, int wc, int fr, int fq) const { if (u.e == 0) rs(acc, u, wr, wc, fr, fq); else cs(acc, u, wr, wc, fr, fq); }
;     __device__ __forceinline__ void operator()(const Acc& acc, const Unit& u, int wr, int wc, int fr, int fq) const {
;         const int col0 = u.pn * 256 + wc * 32 + 8 * fq; const LAS float* sl = slots + (u.idx & 1) * 512 + 256 + wr * 64 + fr;
; #pragma unroll
;         for (int ai = 0; ai < 2; ++ai) {
;             v4u xw[4][2]; float sv[4];
; #pragma unroll
;             for (int m = 0; m < 4; ++m) { const int row = EPI_ROWS(ai, m); const size_t off = (size_t)row * DM + col0; sv[m] = sl[ai * 128 + m * 16];
; #pragma unroll
;                 for (int bj = 0; bj < 2; ++bj) xw[m][bj] = *(const v4u*)(x + off + bj * 128); }
; #pragma unroll
;             for (int m = 0; m < 4; ++m) { const int row = EPI_ROWS(ai, m); const float s = sv[m]; const size_t off = (size_t)row * DM + col0; float q = 0.f;
; #pragma unroll
;                 for (int bj = 0; bj < 2; ++bj) { const v4u w = xw[m][bj];
;                     const f32x4 v0 = (f32x4){__uint_as_float(w.x << 16), __uint_as_float(w.x & 0xffff0000u), __uint_as_float(w.y << 16), __uint_as_float(w.y & 0xffff0000u)} + acc[ai][bj][m][0] * s,
;                                 v1 = (f32x4){__uint_as_float(w.z << 16), __uint_as_float(w.z & 0xffff0000u), __uint_as_float(w.w << 16), __uint_as_float(w.w & 0xffff0000u)} + acc[ai][bj][m][1] * s;
;                     *(v4u*)(x1b + off + bj * 128) = pack8(v0, v1);
;                     q += (v0[0] * v0[0] + v0[1] * v0[1]) + (v0[2] * v0[2] + v0[3] * v0[3]) + (v1[0] * v1[0] + v1[1] * v1[1]) + (v1[2] * v1[2] + v1[3] * v1[3]); }
;                 q += __shfl_xor(q, 16); q += __shfl_xor(q, 32);
;                 if (fq == 0) ss1p[(size_t)row * 32 + u.pn * 4 + wc] = q; } }
.LBB5_1169:
	s_lshl_b32 s8, s29, 8
	v_mov_b32_e32 v2, v184
	v_mov_b32_e32 v178, v185
	s_or_b32 s8, s8, s61
	s_lshl_b32 s0, s0, 8
	s_add_i32 s0, s0, s60
	v_lshl_add_u32 v4, v178, 3, s8
	v_ashrrev_i32_e32 v5, 31, v4
	v_add_u32_e32 v162, s0, v2
	v_lshlrev_b64 v[200:201], 1, v[4:5]
	v_ashrrev_i32_e32 v163, 31, v162
	v_lshl_add_u64 v[160:161], s[10:11], 0, v[200:201]
	v_lshlrev_b64 v[202:203], 12, v[162:163]
	v_lshl_add_u64 v[134:135], v[160:161], 0, v[202:203]
	global_load_dwordx4 v[190:193], v[134:135], off
	global_load_dwordx4 v[194:197], v[134:135], off offset:256
	v_add_u32_e32 v174, 16, v162
	v_add_u32_e32 v168, 32, v162
	v_add_u32_e32 v164, 48, v162
	v_ashrrev_i32_e32 v175, 31, v174
	v_ashrrev_i32_e32 v169, 31, v168
	v_ashrrev_i32_e32 v165, 31, v164
	v_lshlrev_b64 v[176:177], 12, v[174:175]
	v_lshlrev_b64 v[170:171], 12, v[168:169]
	v_lshlrev_b64 v[166:167], 12, v[164:165]
	v_lshl_add_u64 v[134:135], v[160:161], 0, v[176:177]
	v_lshl_add_u64 v[136:137], v[160:161], 0, v[170:171]
	v_lshl_add_u64 v[172:173], v[160:161], 0, v[166:167]
	global_load_dwordx4 v[154:157], v[134:135], off
	global_load_dwordx4 v[150:153], v[134:135], off offset:256
	global_load_dwordx4 v[146:149], v[136:137], off
	global_load_dwordx4 v[142:145], v[136:137], off offset:256
	global_load_dwordx4 v[138:141], v[172:173], off
	s_nop 0
	global_load_dwordx4 v[134:137], v[172:173], off offset:256
	v_add_u32_e32 v250, 0x80, v162
	v_ashrrev_i32_e32 v251, 31, v250
	v_lshlrev_b64 v[248:249], 12, v[250:251]
	v_lshl_add_u64 v[248:249], v[160:161], 0, v[248:249]
	global_load_dwordx4 v[216:219], v[248:249], off
	global_load_dwordx4 v[220:223], v[248:249], off offset:256
	v_add_u32_e32 v250, 0x90, v162
	v_ashrrev_i32_e32 v251, 31, v250
	v_lshlrev_b64 v[248:249], 12, v[250:251]
	v_lshl_add_u64 v[248:249], v[160:161], 0, v[248:249]
	global_load_dwordx4 v[224:227], v[248:249], off
	global_load_dwordx4 v[228:231], v[248:249], off offset:256
	v_add_u32_e32 v250, 0xa0, v162
	v_ashrrev_i32_e32 v251, 31, v250
	v_lshlrev_b64 v[248:249], 12, v[250:251]
	v_lshl_add_u64 v[248:249], v[160:161], 0, v[248:249]
	global_load_dwordx4 v[232:235], v[248:249], off
	global_load_dwordx4 v[236:239], v[248:249], off offset:256
	v_add_u32_e32 v250, 0xb0, v162
	v_ashrrev_i32_e32 v251, 31, v250
	v_lshlrev_b64 v[248:249], 12, v[250:251]
	v_lshl_add_u64 v[248:249], v[160:161], 0, v[248:249]
	global_load_dwordx4 v[240:243], v[248:249], off
	global_load_dwordx4 v[244:247], v[248:249], off offset:256
	s_add_i32 s0, s65, s1
	v_lshl_add_u32 v2, v2, 2, s0
	v_and_b32_e32 v172, 64, v188
	v_add_u32_e32 v189, 0x400, v2
	v_add_u32_e32 v215, 64, v172
	v_cmp_eq_u32_e32 vcc, 0, v178
	ds_read2_b32 v[178:179], v189 offset1:16
	ds_read2_b32 v[172:173], v189 offset0:32 offset1:48
	v_xor_b32_e32 v214, 16, v188
	v_cmp_lt_i32_e64 s[0:1], v214, v215
	s_waitcnt vmcnt(8)
	v_lshlrev_b32_e32 v204, 16, v190
	v_and_b32_e32 v205, 0xffff0000, v190
	v_lshlrev_b32_e32 v190, 16, v191
	v_and_b32_e32 v191, 0xffff0000, v191
	v_lshlrev_b32_e32 v208, 16, v194
	v_and_b32_e32 v209, 0xffff0000, v194
	v_lshlrev_b32_e32 v194, 16, v195
	v_and_b32_e32 v195, 0xffff0000, v195
	v_lshlrev_b32_e32 v206, 16, v192
	v_and_b32_e32 v207, 0xffff0000, v192
	v_lshlrev_b32_e32 v192, 16, v193
	v_and_b32_e32 v193, 0xffff0000, v193
	v_lshlrev_b32_e32 v210, 16, v196
	v_and_b32_e32 v211, 0xffff0000, v196
	v_lshlrev_b32_e32 v196, 16, v197
	v_and_b32_e32 v197, 0xffff0000, v197
	s_waitcnt lgkmcnt(1)
	v_pk_fma_f32 v[132:133], v[132:133], v[178:179], v[190:191] op_sel_hi:[1,0,1]
	v_pk_fma_f32 v[130:131], v[130:131], v[178:179], v[204:205] op_sel_hi:[1,0,1]
	v_pk_fma_f32 v[124:125], v[124:125], v[178:179], v[194:195] op_sel_hi:[1,0,1]
	v_pk_fma_f32 v[122:123], v[122:123], v[178:179], v[208:209] op_sel_hi:[1,0,1]
	v_pk_fma_f32 v[128:129], v[128:129], v[178:179], v[192:193] op_sel_hi:[1,0,1]
	v_pk_fma_f32 v[126:127], v[126:127], v[178:179], v[206:207] op_sel_hi:[1,0,1]
	v_pk_fma_f32 v[190:191], v[120:121], v[178:179], v[196:197] op_sel_hi:[1,0,1]
	v_pk_fma_f32 v[192:193], v[118:119], v[178:179], v[210:211] op_sel_hi:[1,0,1]
	v_cvt_pk_bf16_f32 v118, v130, v131
	v_cvt_pk_bf16_f32 v119, v132, v133
	v_mul_f32_e32 v2, v131, v131
	v_mul_f32_e32 v131, v133, v133
	v_mul_f32_e32 v133, v123, v123
	v_mul_f32_e32 v178, v125, v125
	v_cvt_pk_bf16_f32 v120, v126, v127
	v_mul_f32_e32 v127, v127, v127
	v_mul_f32_e32 v194, v193, v193
	v_fmac_f32_e32 v2, v130, v130
	v_fmac_f32_e32 v131, v132, v132
	v_fmac_f32_e32 v133, v122, v122
	v_fmac_f32_e32 v178, v124, v124
	v_cvt_pk_bf16_f32 v121, v128, v129
	v_mul_f32_e32 v129, v129, v129
	v_mul_f32_e32 v195, v191, v191
	v_fmac_f32_e32 v127, v126, v126
	v_fmac_f32_e32 v194, v192, v192
	v_add_f32_e32 v2, v2, v131
	v_add_f32_e32 v126, v133, v178
	v_fmac_f32_e32 v129, v128, v128
	v_fmac_f32_e32 v195, v190, v190
	v_add_f32_e32 v2, v127, v2
	v_add_f32_e32 v126, v194, v126
	v_add_f32_e32 v2, v129, v2
	v_add_f32_e32 v126, v195, v126
	v_add_f32_e32 v128, v2, v126
	v_cndmask_b32_e64 v2, v188, v214, s[0:1]
	v_lshlrev_b32_e32 v2, 2, v2
	ds_bpermute_b32 v129, v2, v128
	v_lshl_add_u64 v[126:127], s[12:13], 0, v[202:203]
	v_lshl_add_u64 v[126:127], v[126:127], 0, v[200:201]
	global_store_dwordx4 v[126:127], v[118:121], off
	v_cvt_pk_bf16_f32 v122, v122, v123
	v_cvt_pk_bf16_f32 v123, v124, v125
	v_cvt_pk_bf16_f32 v124, v192, v193
	v_cvt_pk_bf16_f32 v125, v190, v191
	global_store_dwordx4 v[126:127], v[122:125], off offset:256
	s_nop 0
	v_xor_b32_e32 v118, 32, v188
	v_cmp_lt_i32_e64 s[0:1], v118, v215
	s_waitcnt lgkmcnt(0)
	v_add_f32_e32 v119, v128, v129
	v_cndmask_b32_e64 v118, v188, v118, s[0:1]
	v_lshlrev_b32_e32 v118, 2, v118
	ds_bpermute_b32 v120, v118, v119
	s_and_saveexec_b64 s[0:1], vcc
	s_cbranch_execz .LBB5_1171
	s_waitcnt lgkmcnt(0)
	v_add_f32_e32 v119, v119, v120
	s_lshl_b32 s46, s29, 2
	v_lshlrev_b64 v[120:121], 7, v[162:163]
	s_ashr_i32 s47, s46, 31
	v_lshl_add_u64 v[120:121], s[14:15], 0, v[120:121]
	v_lshl_add_u64 v[120:121], s[46:47], 2, v[120:121]
	s_lshl_b32 s8, s59, 2
	v_lshl_add_u64 v[120:121], v[120:121], 0, s[8:9]
	global_store_dword v[120:121], v119, off

; __device__ __forceinline__ v4u pack8(const f32x4 a, const f32x4 b) { v4u w; w.x = cvt_pk_bf16(a[0], a[1]); w.y = cvt_pk_bf16(a[2], a[3]); w.z = cvt_pk_bf16(b[0], b[1]); w.w = cvt_pk_bf16(b[2], b[3]); return w; }
;     __device__ __forceinline__ void operator()(const Acc& acc, const Unit& u, int wr, int wc, int fr, int fq) const {
;     ...
;         for (int ai = 0; ai < 2; ++ai) {
;             v4u xw[4][2]; float sv[4];
; #pragma unroll
;             for (int m = 0; m < 4; ++m) { const int row = EPI_ROWS(ai, m); const size_t off = (size_t)row * DM + col0; sv[m] = sl[ai * 128 + m * 16];
; #pragma unroll
;                 for (int bj = 0; bj < 2; ++bj) xw[m][bj] = *(const v4u*)(x + off + bj * 128); }
; #pragma unroll
;             for (int m = 0; m < 4; ++m) { const int row = EPI_ROWS(ai, m); const float s = sv[m]; const size_t off = (size_t)row * DM + col0; float q = 0.f;
; #pragma unroll
;                 for (int bj = 0; bj < 2; ++bj) { const v4u w = xw[m][bj];
;                     const f32x4 v0 = (f32x4){__uint_as_float(w.x << 16), __uint_as_float(w.x & 0xffff0000u), __uint_as_float(w.y << 16), __uint_as_float(w.y & 0xffff0000u)} + acc[ai][bj][m][0] * s,
;                                 v1 = (f32x4){__uint_as_float(w.z << 16), __uint_as_float(w.z & 0xffff0000u), __uint_as_float(w.w << 16), __uint_as_float(w.w & 0xffff0000u)} + acc[ai][bj][m][1] * s;
;                     *(v4u*)(x1b + off + bj * 128) = pack8(v0, v1);
;                     q += (v0[0] * v0[0] + v0[1] * v0[1]) + (v0[2] * v0[2] + v0[3] * v0[3]) + (v1[0] * v1[0] + v1[1] * v1[1]) + (v1[2] * v1[2] + v1[3] * v1[3]); }
;                 q += __shfl_xor(q, 16); q += __shfl_xor(q, 32);
;                 if (fq == 0) ss1p[(size_t)row * 32 + u.pn * 4 + wc] = q; } }
.LBB5_1177:
	s_or_b64 exec, exec, s[0:1]
	v_add_u32_e32 v108, 0x80, v162
	v_ashrrev_i32_e32 v109, 31, v108
	v_lshlrev_b64 v[116:117], 12, v[108:109]
	s_waitcnt lgkmcnt(0)
	v_add_u32_e32 v104, 0x90, v162
	v_add_u32_e32 v98, 0xa0, v162
	v_add_u32_e32 v94, 0xb0, v162
	v_ashrrev_i32_e32 v105, 31, v104
	v_ashrrev_i32_e32 v99, 31, v98
	v_ashrrev_i32_e32 v95, 31, v94
	v_lshlrev_b64 v[106:107], 12, v[104:105]
	v_lshlrev_b64 v[102:103], 12, v[98:99]
	v_lshlrev_b64 v[96:97], 12, v[94:95]
	ds_read2_b32 v[110:111], v189 offset0:128 offset1:144
	ds_read2_b32 v[100:101], v189 offset0:160 offset1:176
	s_waitcnt vmcnt(8)
	v_lshlrev_b32_e32 v124, 16, v216
	v_and_b32_e32 v125, 0xffff0000, v216
	v_lshlrev_b32_e32 v112, 16, v217
	v_and_b32_e32 v113, 0xffff0000, v217
	v_lshlrev_b32_e32 v128, 16, v220
	v_and_b32_e32 v129, 0xffff0000, v220
	v_lshlrev_b32_e32 v120, 16, v221
	v_and_b32_e32 v121, 0xffff0000, v221
	v_lshlrev_b32_e32 v126, 16, v218
	v_and_b32_e32 v127, 0xffff0000, v218
	v_lshlrev_b32_e32 v114, 16, v219
	v_and_b32_e32 v115, 0xffff0000, v219
	v_lshlrev_b32_e32 v130, 16, v222
	v_and_b32_e32 v131, 0xffff0000, v222
	v_lshlrev_b32_e32 v122, 16, v223
	v_and_b32_e32 v123, 0xffff0000, v223
	s_waitcnt lgkmcnt(1)
	v_pk_fma_f32 v[68:69], v[68:69], v[110:111], v[112:113] op_sel_hi:[1,0,1]
	v_pk_fma_f32 v[66:67], v[66:67], v[110:111], v[124:125] op_sel_hi:[1,0,1]
	v_pk_fma_f32 v[60:61], v[60:61], v[110:111], v[120:121] op_sel_hi:[1,0,1]
	v_pk_fma_f32 v[58:59], v[58:59], v[110:111], v[128:129] op_sel_hi:[1,0,1]
	v_pk_fma_f32 v[64:65], v[64:65], v[110:111], v[114:115] op_sel_hi:[1,0,1]
	v_pk_fma_f32 v[62:63], v[62:63], v[110:111], v[126:127] op_sel_hi:[1,0,1]
	v_pk_fma_f32 v[112:113], v[56:57], v[110:111], v[122:123] op_sel_hi:[1,0,1]
	v_pk_fma_f32 v[114:115], v[54:55], v[110:111], v[130:131] op_sel_hi:[1,0,1]
	v_cvt_pk_bf16_f32 v54, v66, v67
	v_cvt_pk_bf16_f32 v55, v68, v69
	v_mul_f32_e32 v67, v67, v67
	v_mul_f32_e32 v69, v69, v69
	v_mul_f32_e32 v110, v59, v59
	v_mul_f32_e32 v119, v61, v61
	v_cvt_pk_bf16_f32 v56, v62, v63
	v_cvt_pk_bf16_f32 v57, v64, v65
	v_mul_f32_e32 v63, v63, v63
	v_mul_f32_e32 v65, v65, v65
	v_mul_f32_e32 v120, v115, v115
	v_fmac_f32_e32 v67, v66, v66
	v_fmac_f32_e32 v69, v68, v68
	v_fmac_f32_e32 v110, v58, v58
	v_fmac_f32_e32 v119, v60, v60
	v_mul_f32_e32 v121, v113, v113
	v_fmac_f32_e32 v63, v62, v62
	v_fmac_f32_e32 v65, v64, v64
	v_fmac_f32_e32 v120, v114, v114
	v_add_f32_e32 v62, v67, v69
	v_add_f32_e32 v64, v110, v119
	v_fmac_f32_e32 v121, v112, v112
	v_add_f32_e32 v62, v63, v62
	v_add_f32_e32 v63, v120, v64
	v_add_f32_e32 v62, v65, v62
	v_add_f32_e32 v63, v121, v63
	v_add_f32_e32 v64, v62, v63
	ds_bpermute_b32 v65, v2, v64
	v_lshl_add_u64 v[62:63], s[12:13], 0, v[116:117]
	v_lshl_add_u64 v[62:63], v[4:5], 1, v[62:63]
	global_store_dwordx4 v[62:63], v[54:57], off
	s_waitcnt lgkmcnt(0)
	s_nop 0
	v_add_f32_e32 v54, v64, v65
	ds_bpermute_b32 v55, v118, v54
	v_cvt_pk_bf16_f32 v56, v58, v59
	v_cvt_pk_bf16_f32 v57, v60, v61
	v_cvt_pk_bf16_f32 v58, v114, v115
	v_cvt_pk_bf16_f32 v59, v112, v113
	global_store_dwordx4 v[62:63], v[56:59], off offset:256
	s_and_saveexec_b64 s[0:1], vcc
	s_cbranch_execz .LBB5_1179
	s_waitcnt lgkmcnt(0)
	v_add_f32_e32 v56, v54, v55
	s_lshl_b32 s46, s29, 2
	v_lshlrev_b64 v[54:55], 7, v[108:109]
	s_ashr_i32 s47, s46, 31
	v_lshl_add_u64 v[54:55], s[14:15], 0, v[54:55]
	v_lshl_add_u64 v[54:55], s[46:47], 2, v[54:55]
	s_lshl_b32 s8, s59, 2
	v_lshl_add_u64 v[54:55], v[54:55], 0, s[8:9]
	global_store_dword v[54:55], v56, off
.LBB5_1179:
	s_or_b64 exec, exec, s[0:1]
	v_lshlrev_b32_e32 v54, 16, v224
	s_waitcnt lgkmcnt(0)
	v_and_b32_e32 v55, 0xffff0000, v224
	v_mov_b32_e32 v58, v111
	v_lshlrev_b32_e32 v56, 16, v225
	v_and_b32_e32 v57, 0xffff0000, v225
	v_pk_fma_f32 v[50:51], v[50:51], v[58:59], v[54:55] op_sel_hi:[1,0,1]
	v_lshlrev_b32_e32 v54, 16, v226
	v_and_b32_e32 v55, 0xffff0000, v226
	v_pk_fma_f32 v[52:53], v[52:53], v[58:59], v[56:57] op_sel_hi:[1,0,1]
	v_pk_fma_f32 v[54:55], v[46:47], v[58:59], v[54:55] op_sel_hi:[1,0,1]
	v_cvt_pk_bf16_f32 v46, v50, v51
	v_mul_f32_e32 v51, v51, v51
	v_fmac_f32_e32 v51, v50, v50
	v_mul_f32_e32 v50, v53, v53
	v_fmac_f32_e32 v50, v52, v52
	v_lshlrev_b32_e32 v56, 16, v227
	v_and_b32_e32 v57, 0xffff0000, v227
	v_add_f32_e32 v50, v51, v50
	v_mul_f32_e32 v51, v55, v55
	v_pk_fma_f32 v[56:57], v[48:49], v[58:59], v[56:57] op_sel_hi:[1,0,1]
	v_fmac_f32_e32 v51, v54, v54
	v_add_f32_e32 v50, v51, v50
	v_mul_f32_e32 v51, v57, v57
	v_fmac_f32_e32 v51, v56, v56
	v_cvt_pk_bf16_f32 v47, v52, v53
	v_cvt_pk_bf16_f32 v48, v54, v55
	v_add_f32_e32 v54, v51, v50
	v_lshlrev_b32_e32 v50, 16, v228
	v_and_b32_e32 v51, 0xffff0000, v228
	v_lshlrev_b32_e32 v52, 16, v229
	v_and_b32_e32 v53, 0xffff0000, v229
	v_pk_fma_f32 v[44:45], v[44:45], v[58:59], v[52:53] op_sel_hi:[1,0,1]
	v_pk_fma_f32 v[42:43], v[42:43], v[58:59], v[50:51] op_sel_hi:[1,0,1]
	v_lshlrev_b32_e32 v50, 16, v230
	v_and_b32_e32 v51, 0xffff0000, v230
	v_pk_fma_f32 v[50:51], v[38:39], v[58:59], v[50:51] op_sel_hi:[1,0,1]
	v_mul_f32_e32 v38, v43, v43
	v_mul_f32_e32 v39, v45, v45
	v_fmac_f32_e32 v38, v42, v42
	v_fmac_f32_e32 v39, v44, v44
	v_lshlrev_b32_e32 v52, 16, v231
	v_and_b32_e32 v53, 0xffff0000, v231
	v_add_f32_e32 v38, v38, v39
	v_mul_f32_e32 v39, v51, v51
	v_pk_fma_f32 v[52:53], v[40:41], v[58:59], v[52:53] op_sel_hi:[1,0,1]
	v_fmac_f32_e32 v39, v50, v50
	v_add_f32_e32 v38, v39, v38
	v_mul_f32_e32 v39, v53, v53
	v_fmac_f32_e32 v39, v52, v52
	v_add_f32_e32 v38, v39, v38
	v_add_f32_e32 v41, v54, v38
	v_cvt_pk_bf16_f32 v49, v56, v57
	ds_bpermute_b32 v56, v2, v41
	v_lshl_add_u64 v[38:39], s[12:13], 0, v[106:107]
	v_lshl_add_u64 v[54:55], v[4:5], 1, v[38:39]
	global_store_dwordx4 v[54:55], v[46:49], off
	v_cvt_pk_bf16_f32 v40, v42, v43
	s_waitcnt lgkmcnt(0)
	v_add_f32_e32 v38, v41, v56
	ds_bpermute_b32 v39, v118, v38
	v_cvt_pk_bf16_f32 v41, v44, v45
	v_cvt_pk_bf16_f32 v42, v50, v51
	v_cvt_pk_bf16_f32 v43, v52, v53
	global_store_dwordx4 v[54:55], v[40:43], off offset:256
	s_and_saveexec_b64 s[0:1], vcc
	s_cbranch_execz .LBB5_1181
	s_waitcnt lgkmcnt(0)
	v_add_f32_e32 v40, v38, v39
	s_lshl_b32 s46, s29, 2
	v_lshlrev_b64 v[38:39], 7, v[104:105]
	s_ashr_i32 s47, s46, 31
	v_lshl_add_u64 v[38:39], s[14:15], 0, v[38:39]
	v_lshl_add_u64 v[38:39], s[46:47], 2, v[38:39]
	s_lshl_b32 s8, s59, 2
	v_lshl_add_u64 v[38:39], v[38:39], 0, s[8:9]
	global_store_dword v[38:39], v40, off
; __device__ __forceinline__ v4u pack8(const f32x4 a, const f32x4 b) { v4u w; w.x = cvt_pk_bf16(a[0], a[1]); w.y = cvt_pk_bf16(a[2], a[3]); w.z = cvt_pk_bf16(b[0], b[1]); w.w = cvt_pk_bf16(b[2], b[3]); return w; }
;     __device__ __forceinline__ void operator()(const Acc& acc, const Unit& u, int wr, int wc, int fr, int fq) const {
;     ...
;             for (int m = 0; m < 4; ++m) { const int row = EPI_ROWS(ai, m); const float s = sv[m]; const size_t off = (size_t)row * DM + col0; float q = 0.f;
; #pragma unroll
;                 for (int bj = 0; bj < 2; ++bj) { const v4u w = xw[m][bj];
;                     const f32x4 v0 = (f32x4){__uint_as_float(w.x << 16), __uint_as_float(w.x & 0xffff0000u), __uint_as_float(w.y << 16), __uint_as_float(w.y & 0xffff0000u)} + acc[ai][bj][m][0] * s,
;                                 v1 = (f32x4){__uint_as_float(w.z << 16), __uint_as_float(w.z & 0xffff0000u), __uint_as_float(w.w << 16), __uint_as_float(w.w & 0xffff0000u)} + acc[ai][bj][m][1] * s;
;                     *(v4u*)(x1b + off + bj * 128) = pack8(v0, v1);
;                     q += (v0[0] * v0[0] + v0[1] * v0[1]) + (v0[2] * v0[2] + v0[3] * v0[3]) + (v1[0] * v1[0] + v1[1] * v1[1]) + (v1[2] * v1[2] + v1[3] * v1[3]); }
;                 q += __shfl_xor(q, 16); q += __shfl_xor(q, 32);
;                 if (fq == 0) ss1p[(size_t)row * 32 + u.pn * 4 + wc] = q; } }
.LBB5_1181:
	s_or_b64 exec, exec, s[0:1]
	v_lshlrev_b32_e32 v38, 16, v232
	s_waitcnt lgkmcnt(0)
	v_and_b32_e32 v39, 0xffff0000, v232
	v_lshlrev_b32_e32 v40, 16, v233
	v_and_b32_e32 v41, 0xffff0000, v233
	v_pk_fma_f32 v[34:35], v[34:35], v[100:101], v[38:39] op_sel_hi:[1,0,1]
	v_lshlrev_b32_e32 v38, 16, v234
	v_and_b32_e32 v39, 0xffff0000, v234
	v_pk_fma_f32 v[36:37], v[36:37], v[100:101], v[40:41] op_sel_hi:[1,0,1]
	v_pk_fma_f32 v[38:39], v[30:31], v[100:101], v[38:39] op_sel_hi:[1,0,1]
	v_cvt_pk_bf16_f32 v30, v34, v35
	v_mul_f32_e32 v35, v35, v35
	v_fmac_f32_e32 v35, v34, v34
	v_mul_f32_e32 v34, v37, v37
	v_fmac_f32_e32 v34, v36, v36
	v_lshlrev_b32_e32 v40, 16, v235
	v_and_b32_e32 v41, 0xffff0000, v235
	v_add_f32_e32 v34, v35, v34
	v_mul_f32_e32 v35, v39, v39
	v_pk_fma_f32 v[40:41], v[32:33], v[100:101], v[40:41] op_sel_hi:[1,0,1]
	v_fmac_f32_e32 v35, v38, v38
	v_add_f32_e32 v34, v35, v34
	v_mul_f32_e32 v35, v41, v41
	v_fmac_f32_e32 v35, v40, v40
	v_cvt_pk_bf16_f32 v31, v36, v37
	v_cvt_pk_bf16_f32 v32, v38, v39
	v_add_f32_e32 v38, v35, v34
	v_lshlrev_b32_e32 v34, 16, v236
	v_and_b32_e32 v35, 0xffff0000, v236
	v_lshlrev_b32_e32 v36, 16, v237
	v_and_b32_e32 v37, 0xffff0000, v237
	v_pk_fma_f32 v[28:29], v[28:29], v[100:101], v[36:37] op_sel_hi:[1,0,1]
	v_pk_fma_f32 v[26:27], v[26:27], v[100:101], v[34:35] op_sel_hi:[1,0,1]
	v_lshlrev_b32_e32 v34, 16, v238
	v_and_b32_e32 v35, 0xffff0000, v238
	v_pk_fma_f32 v[34:35], v[22:23], v[100:101], v[34:35] op_sel_hi:[1,0,1]
	v_mul_f32_e32 v22, v27, v27
	v_mul_f32_e32 v23, v29, v29
	v_fmac_f32_e32 v22, v26, v26
	v_fmac_f32_e32 v23, v28, v28
	v_lshlrev_b32_e32 v36, 16, v239
	v_and_b32_e32 v37, 0xffff0000, v239
	v_add_f32_e32 v22, v22, v23
	v_mul_f32_e32 v23, v35, v35
	v_pk_fma_f32 v[36:37], v[24:25], v[100:101], v[36:37] op_sel_hi:[1,0,1]
	v_fmac_f32_e32 v23, v34, v34
	v_add_f32_e32 v22, v23, v22
	v_mul_f32_e32 v23, v37, v37
	v_fmac_f32_e32 v23, v36, v36
	v_add_f32_e32 v22, v23, v22
	v_add_f32_e32 v25, v38, v22
	v_cvt_pk_bf16_f32 v33, v40, v41
	ds_bpermute_b32 v40, v2, v25
	v_lshl_add_u64 v[22:23], s[12:13], 0, v[102:103]
	v_lshl_add_u64 v[38:39], v[4:5], 1, v[22:23]
	global_store_dwordx4 v[38:39], v[30:33], off
	v_cvt_pk_bf16_f32 v24, v26, v27
	s_waitcnt lgkmcnt(0)
	v_add_f32_e32 v22, v25, v40
	ds_bpermute_b32 v23, v118, v22
	v_cvt_pk_bf16_f32 v25, v28, v29
	v_cvt_pk_bf16_f32 v26, v34, v35
	v_cvt_pk_bf16_f32 v27, v36, v37
	global_store_dwordx4 v[38:39], v[24:27], off offset:256
	s_and_saveexec_b64 s[0:1], vcc
	s_cbranch_execz .LBB5_1183
	s_waitcnt lgkmcnt(0)
	v_add_f32_e32 v24, v22, v23
	s_lshl_b32 s46, s29, 2
	v_lshlrev_b64 v[22:23], 7, v[98:99]
	s_ashr_i32 s47, s46, 31
	v_lshl_add_u64 v[22:23], s[14:15], 0, v[22:23]
	v_lshl_add_u64 v[22:23], s[46:47], 2, v[22:23]
	s_lshl_b32 s8, s59, 2
	v_lshl_add_u64 v[22:23], v[22:23], 0, s[8:9]
	global_store_dword v[22:23], v24, off
.LBB5_1183:
	s_or_b64 exec, exec, s[0:1]
	v_lshlrev_b32_e32 v22, 16, v240
	s_waitcnt lgkmcnt(0)
	v_and_b32_e32 v23, 0xffff0000, v240
	v_mov_b32_e32 v26, v101
	v_lshlrev_b32_e32 v24, 16, v241
	v_and_b32_e32 v25, 0xffff0000, v241
	v_pk_fma_f32 v[18:19], v[18:19], v[26:27], v[22:23] op_sel_hi:[1,0,1]
	v_lshlrev_b32_e32 v22, 16, v242
	v_and_b32_e32 v23, 0xffff0000, v242
	v_pk_fma_f32 v[20:21], v[20:21], v[26:27], v[24:25] op_sel_hi:[1,0,1]
	v_pk_fma_f32 v[22:23], v[14:15], v[26:27], v[22:23] op_sel_hi:[1,0,1]
	v_cvt_pk_bf16_f32 v14, v18, v19
	v_mul_f32_e32 v19, v19, v19
	v_fmac_f32_e32 v19, v18, v18
	v_mul_f32_e32 v18, v21, v21
	v_fmac_f32_e32 v18, v20, v20
	v_lshlrev_b32_e32 v24, 16, v243
	v_and_b32_e32 v25, 0xffff0000, v243
	v_add_f32_e32 v18, v19, v18
	v_mul_f32_e32 v19, v23, v23
	v_pk_fma_f32 v[24:25], v[16:17], v[26:27], v[24:25] op_sel_hi:[1,0,1]
	v_fmac_f32_e32 v19, v22, v22
	v_add_f32_e32 v18, v19, v18
	v_mul_f32_e32 v19, v25, v25
	v_fmac_f32_e32 v19, v24, v24
	v_cvt_pk_bf16_f32 v15, v20, v21
	v_cvt_pk_bf16_f32 v16, v22, v23
	v_add_f32_e32 v22, v19, v18
	v_lshlrev_b32_e32 v18, 16, v244
	v_and_b32_e32 v19, 0xffff0000, v244
	v_lshlrev_b32_e32 v20, 16, v245
	v_and_b32_e32 v21, 0xffff0000, v245
	v_pk_fma_f32 v[12:13], v[12:13], v[26:27], v[20:21] op_sel_hi:[1,0,1]
	v_pk_fma_f32 v[10:11], v[10:11], v[26:27], v[18:19] op_sel_hi:[1,0,1]
	v_lshlrev_b32_e32 v18, 16, v246
	v_and_b32_e32 v19, 0xffff0000, v246
	v_lshlrev_b32_e32 v20, 16, v247
	v_and_b32_e32 v21, 0xffff0000, v247
	v_pk_fma_f32 v[20:21], v[8:9], v[26:27], v[20:21] op_sel_hi:[1,0,1]
	v_pk_fma_f32 v[8:9], v[6:7], v[26:27], v[18:19] op_sel_hi:[1,0,1]
	v_mul_f32_e32 v6, v11, v11
	v_mul_f32_e32 v7, v13, v13
	v_fmac_f32_e32 v6, v10, v10
	v_fmac_f32_e32 v7, v12, v12
	v_add_f32_e32 v6, v6, v7
	v_mul_f32_e32 v7, v9, v9
	v_fmac_f32_e32 v7, v8, v8
	v_add_f32_e32 v6, v7, v6
	v_mul_f32_e32 v7, v21, v21
	v_fmac_f32_e32 v7, v20, v20
	v_add_f32_e32 v6, v7, v6
	v_add_f32_e32 v22, v22, v6
	ds_bpermute_b32 v2, v2, v22
	v_lshl_add_u64 v[6:7], s[12:13], 0, v[96:97]
	v_lshl_add_u64 v[18:19], v[4:5], 1, v[6:7]
	v_cvt_pk_bf16_f32 v17, v24, v25
	global_store_dwordx4 v[18:19], v[14:17], off
	s_waitcnt lgkmcnt(0)
	v_add_f32_e32 v2, v22, v2
	ds_bpermute_b32 v4, v118, v2
	v_cvt_pk_bf16_f32 v6, v10, v11
	v_cvt_pk_bf16_f32 v7, v12, v13
	v_cvt_pk_bf16_f32 v8, v8, v9
	v_cvt_pk_bf16_f32 v9, v20, v21
	global_store_dwordx4 v[18:19], v[6:9], off offset:256
	s_and_saveexec_b64 s[0:1], vcc
	s_cbranch_execz .LBB5_1185
	s_waitcnt lgkmcnt(0)
	v_add_f32_e32 v2, v2, v4
	s_lshl_b32 s46, s29, 2
	v_lshlrev_b64 v[4:5], 7, v[94:95]
	s_ashr_i32 s47, s46, 31
	v_lshl_add_u64 v[4:5], s[14:15], 0, v[4:5]
	v_lshl_add_u64 v[4:5], s[46:47], 2, v[4:5]
	s_lshl_b32 s8, s59, 2
	v_lshl_add_u64 v[4:5], v[4:5], 0, s[8:9]
	global_store_dword v[4:5], v2, off
